# younger-wave stagger in the thin (norm+residual) phase: waves get a start offset by wave pair (s_sleep 0/30/60/90) so one group's memory phase overlaps another's compute; plus MoBA QK K-fragment prefe
# baseline (speedup 1.0000x reference)
.LBB0_876:
	s_ashr_i32 s4, s4, 6
	s_lshl_b32 s1, s1, 3
	s_add_i32 s68, s1, s4
	v_readlane_b32 s1, v248, 11
	s_add_i32 s43, s1, 1
	s_cmp_eq_u32 s43, 12
	s_cselect_b64 s[4:5], -1, 0
	s_cmp_lg_u32 s43, 12
	s_cselect_b64 s[6:7], -1, 0
	s_cmpk_gt_i32 s68, 0x1fff
	s_cbranch_scc1 .LBB0_928
	v_and_b32_e32 v5, 64, v199
	v_add_u32_e32 v5, 64, v5
	v_xor_b32_e32 v6, 1, v199
	v_cmp_lt_i32_e32 vcc, v6, v5
	s_lshl_b32 s10, s0, 3
	v_readlane_b32 s0, v248, 18
	v_cndmask_b32_e32 v6, v199, v6, vcc
	v_lshlrev_b32_e32 v157, 2, v6
	v_xor_b32_e32 v6, 2, v199
	v_cmp_lt_i32_e32 vcc, v6, v5
	v_readlane_b32 s1, v248, 19
	s_mov_b32 s8, s87
	v_cndmask_b32_e32 v6, v199, v6, vcc
	v_lshlrev_b32_e32 v158, 2, v6
	v_xor_b32_e32 v6, 4, v199
	v_cmp_lt_i32_e32 vcc, v6, v5
	v_cndmask_b32_e64 v156, 0.5, 1.0, s[0:1]
	v_readlane_b32 s0, v248, 12
	v_cndmask_b32_e32 v6, v199, v6, vcc
	v_readlane_b32 s1, v248, 17
	v_lshlrev_b32_e32 v159, 2, v6
	v_xor_b32_e32 v6, 8, v199
	s_add_i32 s0, s0, s1
	s_mov_b32 s1, s86
	v_readlane_b32 s72, v250, 4
	v_cmp_lt_i32_e32 vcc, v6, v5
	s_lshl_b32 s0, s0, 13
	v_readlane_b32 s78, v250, 10
	v_cndmask_b32_e32 v6, v199, v6, vcc
	v_readlane_b32 s76, v250, 8
	v_readlane_b32 s77, v250, 9
	v_readlane_b32 s79, v250, 11
	v_readlane_b32 s80, v250, 12
	v_readlane_b32 s81, v250, 13
	v_readlane_b32 s82, v250, 14
	v_readlane_b32 s83, v250, 15
	v_readlane_b32 s86, v250, 18
	s_add_u32 s0, s78, s0
	v_lshlrev_b32_e32 v160, 2, v6
	v_xor_b32_e32 v6, 16, v199
	v_and_b32_e32 v4, 63, v2
	v_readlane_b32 s87, v250, 19
	s_mov_b32 s86, s1
	s_addc_u32 s1, s79, 0
	v_readlane_b32 s76, v249, 55
	v_readlane_b32 s12, v250, 20
	v_cmp_lt_i32_e32 vcc, v6, v5
	s_mov_b32 s87, s8
	v_readlane_b32 s80, v249, 59
	v_readlane_b32 s81, v249, 60
	s_and_b64 s[8:9], s[4:5], exec
	v_lshlrev_b32_e32 v2, 4, v4
	v_readlane_b32 s13, v250, 21
	v_cndmask_b32_e32 v6, v199, v6, vcc
	s_cselect_b32 s9, s81, 0
	s_cselect_b32 s8, s80, 0
	v_lshl_add_u64 v[100:101], s[90:91], 0, v[2:3]
	v_lshl_add_u64 v[102:103], s[12:13], 0, v[2:3]
	v_lshlrev_b32_e32 v2, 5, v4
	v_lshlrev_b32_e32 v161, 2, v6
	v_xor_b32_e32 v6, 32, v199
	v_readlane_b32 s77, v249, 56
	v_lshl_add_u64 v[104:105], s[0:1], 0, v[2:3]
	s_mov_b64 s[0:1], 0x1000
	v_cmp_lt_i32_e32 vcc, v6, v5
	s_cmp_lg_u64 s[8:9], 0
	v_readlane_b32 s73, v250, 5
	v_readlane_b32 s84, v250, 16
	v_readlane_b32 s85, v250, 17
	v_readlane_b32 s78, v249, 57
	v_readlane_b32 s79, v249, 58
	v_readlane_b32 s76, v250, 22
	v_lshl_add_u64 v[106:107], v[104:105], 0, s[0:1]
	s_mov_b64 s[0:1], 0x1800
	v_cndmask_b32_e32 v5, v199, v6, vcc
	s_cselect_b64 s[62:63], -1, 0
	v_cmp_ne_u32_e32 vcc, 0, v4
	v_readlane_b32 s72, v248, 9
	v_readlane_b32 s84, v248, 3
	v_readlane_b32 s78, v249, 63
	v_readlane_b32 s77, v250, 23
	v_readlane_b32 s80, v248, 1
	v_lshl_add_u64 v[108:109], v[104:105], 0, s[0:1]
	v_lshl_add_u64 v[110:111], s[8:9], 0, v[2:3]
	s_or_b64 s[0:1], s[62:63], vcc
	v_lshlrev_b32_e32 v2, 3, v4
	v_readlane_b32 s73, v248, 10
	v_readlane_b32 s85, v248, 4
	v_readlane_b32 s82, v249, 61
	v_readlane_b32 s83, v249, 62
	v_readlane_b32 s79, v248, 0
	v_readlane_b32 s81, v248, 2
	v_lshlrev_b32_e32 v162, 2, v5
	s_xor_b64 s[64:65], s[0:1], -1
	v_cmp_eq_u32_e64 s[36:37], 0, v4
	v_lshl_add_u64 v[112:113], s[76:77], 0, v[2:3]
	v_readlane_b32 s74, v250, 6
	v_readlane_b32 s75, v250, 7
	v_readfirstlane_b32 s100, v0
	s_nop 3
	s_lshr_b32 s100, s100, 6
	s_and_b32 s101, s100, 4
	s_cmp_eq_u32 s101, 0
	s_cbranch_scc1 .Lthin_s1
	s_sleep 60
.Lthin_s1:
	s_and_b32 s101, s100, 2
	s_cmp_eq_u32 s101, 0
	s_cbranch_scc1 .Lthin_nosleep
	s_sleep 30
.Lthin_nosleep:
	s_branch .LBB0_880
.LBB0_878:
	s_or_b64 exec, exec, s[8:9]

	.amdhsa_kernel _Z9trunk_fwd4Args
		.amdhsa_group_segment_fixed_size 0
		.amdhsa_private_segment_fixed_size 0
		.amdhsa_kernarg_size 352
		.amdhsa_user_sgpr_count 2
		.amdhsa_user_sgpr_dispatch_ptr 0
		.amdhsa_user_sgpr_queue_ptr 0
		.amdhsa_user_sgpr_kernarg_segment_ptr 1
		.amdhsa_user_sgpr_dispatch_id 0
		.amdhsa_user_sgpr_kernarg_preload_length 0
		.amdhsa_user_sgpr_kernarg_preload_offset 0
		.amdhsa_user_sgpr_private_segment_size 0
		.amdhsa_uses_dynamic_stack 0
		.amdhsa_enable_private_segment 0
		.amdhsa_system_sgpr_workgroup_id_x 1
		.amdhsa_system_sgpr_workgroup_id_y 0
		.amdhsa_system_sgpr_workgroup_id_z 0
		.amdhsa_system_sgpr_workgroup_info 0
		.amdhsa_system_vgpr_workitem_id 0
		.amdhsa_next_free_vgpr 251
		.amdhsa_next_free_sgpr 102
		.amdhsa_accum_offset 252
		.amdhsa_reserve_vcc 1
		.amdhsa_float_round_mode_32 0
		.amdhsa_float_round_mode_16_64 0
		.amdhsa_float_denorm_mode_32 3
		.amdhsa_float_denorm_mode_16_64 3
		.amdhsa_dx10_clamp 1
		.amdhsa_ieee_mode 1
		.amdhsa_fp16_overflow 0
		.amdhsa_tg_split 0
		.amdhsa_exception_fp_ieee_invalid_op 0
		.amdhsa_exception_fp_denorm_src 0
		.amdhsa_exception_fp_ieee_div_zero 0
		.amdhsa_exception_fp_ieee_overflow 0
		.amdhsa_exception_fp_ieee_underflow 0
		.amdhsa_exception_fp_ieee_inexact 0
		.amdhsa_exception_int_div_zero 0
	.end_amdhsa_kernel

amdhsa.kernels:
  - .agpr_count:     0
    .args:
      - .offset:         0
        .size:           96
        .value_kind:     by_value
      - .offset:         96
        .size:           4
        .value_kind:     hidden_block_count_x
      - .offset:         100
        .size:           4
        .value_kind:     hidden_block_count_y
      - .offset:         104
        .size:           4
        .value_kind:     hidden_block_count_z
      - .offset:         108
        .size:           2
        .value_kind:     hidden_group_size_x
      - .offset:         110
        .size:           2
        .value_kind:     hidden_group_size_y
      - .offset:         112
        .size:           2
        .value_kind:     hidden_group_size_z
      - .offset:         114
        .size:           2
        .value_kind:     hidden_remainder_x
      - .offset:         116
        .size:           2
        .value_kind:     hidden_remainder_y
      - .offset:         118
        .size:           2
        .value_kind:     hidden_remainder_z
      - .offset:         136
        .size:           8
        .value_kind:     hidden_global_offset_x
      - .offset:         144
        .size:           8
        .value_kind:     hidden_global_offset_y
      - .offset:         152
        .size:           8
        .value_kind:     hidden_global_offset_z
      - .offset:         160
        .size:           2
        .value_kind:     hidden_grid_dims
      - .offset:         216
        .size:           4
        .value_kind:     hidden_dynamic_lds_size
    .group_segment_fixed_size: 0
    .kernarg_segment_align: 8
    .kernarg_segment_size: 352
    .language:       OpenCL C
    .language_version:
      - 2
      - 0
    .max_flat_workgroup_size: 512
    .name:           _Z9trunk_fwd4Args
    .private_segment_fixed_size: 0
    .sgpr_count:     108
    .sgpr_spill_count: 148
    .symbol:         _Z9trunk_fwd4Args.kd
    .uniform_work_group_size: 1
    .uses_dynamic_stack: false
    .vgpr_count:     251
    .vgpr_spill_count: 0
    .wavefront_size: 64
